# plus the same DMA split in the two bf16 GEMM K-loops
# speedup vs baseline: 1.0100x; 1.0100x over previous
.LBB0_243:
	ds_read_b128 v[74:77], v201
	ds_read_b128 v[78:81], v201 offset:1024
	ds_read_b128 v[82:85], v201 offset:2048
	ds_read_b128 v[86:89], v201 offset:3072
	ds_read_b128 v[164:167], v202
	ds_read_b128 v[168:171], v202 offset:1024
	ds_read_b128 v[172:175], v202 offset:2048
	ds_read_b128 v[176:179], v202 offset:3072
	s_add_u32 s26, s24, 0xfff80080
	s_addc_u32 s27, s25, -1
	s_cmp_eq_u32 s19, 28
	s_cselect_b32 s29, s21, s27
	s_cselect_b32 s28, s20, s26
	s_cselect_b32 s27, s23, s17
	s_cselect_b32 s26, s22, s7
	v_lshl_add_u64 v[228:229], s[24:25], 0, v[156:157]
	s_add_i32 m0, s41, 0xc000
	ds_read_b128 v[180:183], v203
	ds_read_b128 v[184:187], v203 offset:1024
	ds_read_b128 v[204:207], v203 offset:2048
	ds_read_b128 v[208:211], v203 offset:3072
	ds_read_b128 v[212:215], v203 offset:4096
	ds_read_b128 v[216:219], v203 offset:5120
	ds_read_b128 v[220:223], v203 offset:6144
	ds_read_b128 v[224:227], v203 offset:7168
	global_load_lds_dwordx4 v[228:229], off
	v_lshl_add_u64 v[228:229], s[24:25], 0, v[158:159]
	s_add_i32 m0, s41, 0xe000
	s_nop 0
	global_load_lds_dwordx4 v[228:229], off
	s_waitcnt vmcnt(8)
	s_waitcnt lgkmcnt(0)
	s_barrier
	s_setprio 1
	s_waitcnt lgkmcnt(0)
	v_mfma_f32_16x16x32_bf16 v[142:145], v[74:77], v[180:183], v[142:145]
	v_mfma_f32_16x16x32_bf16 v[138:141], v[82:85], v[180:183], v[138:141]
	v_mfma_f32_16x16x32_bf16 v[126:129], v[74:77], v[204:207], v[126:129]
	v_mfma_f32_16x16x32_bf16 v[122:125], v[82:85], v[204:207], v[122:125]
	v_mfma_f32_16x16x32_bf16 v[110:113], v[74:77], v[212:215], v[110:113]
	v_mfma_f32_16x16x32_bf16 v[106:109], v[82:85], v[212:215], v[106:109]
	v_mfma_f32_16x16x32_bf16 v[94:97], v[74:77], v[220:223], v[94:97]
	v_mfma_f32_16x16x32_bf16 v[90:93], v[82:85], v[220:223], v[90:93]
	v_mfma_f32_16x16x32_bf16 v[142:145], v[78:81], v[184:187], v[142:145]
	v_mfma_f32_16x16x32_bf16 v[138:141], v[86:89], v[184:187], v[138:141]
	v_mfma_f32_16x16x32_bf16 v[126:129], v[78:81], v[208:211], v[126:129]
	v_mfma_f32_16x16x32_bf16 v[122:125], v[86:89], v[208:211], v[122:125]
	v_mfma_f32_16x16x32_bf16 v[110:113], v[78:81], v[216:219], v[110:113]
	v_mfma_f32_16x16x32_bf16 v[106:109], v[86:89], v[216:219], v[106:109]
	v_mfma_f32_16x16x32_bf16 v[94:97], v[78:81], v[224:227], v[94:97]
	v_mfma_f32_16x16x32_bf16 v[90:93], v[86:89], v[224:227], v[90:93]
	s_setprio 0
	s_setprio 1
	v_mfma_f32_16x16x32_bf16 v[134:137], v[164:167], v[180:183], v[134:137]
	v_mfma_f32_16x16x32_bf16 v[130:133], v[172:175], v[180:183], v[130:133]
	v_mfma_f32_16x16x32_bf16 v[118:121], v[164:167], v[204:207], v[118:121]
	v_mfma_f32_16x16x32_bf16 v[114:117], v[172:175], v[204:207], v[114:117]
	v_mfma_f32_16x16x32_bf16 v[102:105], v[164:167], v[212:215], v[102:105]
	v_mfma_f32_16x16x32_bf16 v[98:101], v[172:175], v[212:215], v[98:101]
	v_mfma_f32_16x16x32_bf16 v[70:73], v[164:167], v[220:223], v[70:73]
	v_mfma_f32_16x16x32_bf16 v[66:69], v[172:175], v[220:223], v[66:69]
	v_mfma_f32_16x16x32_bf16 v[134:137], v[168:171], v[184:187], v[134:137]
	v_mfma_f32_16x16x32_bf16 v[130:133], v[176:179], v[184:187], v[130:133]
	v_mfma_f32_16x16x32_bf16 v[118:121], v[168:171], v[208:211], v[118:121]
	v_mfma_f32_16x16x32_bf16 v[114:117], v[176:179], v[208:211], v[114:117]
	v_mfma_f32_16x16x32_bf16 v[102:105], v[168:171], v[216:219], v[102:105]
	v_mfma_f32_16x16x32_bf16 v[98:101], v[176:179], v[216:219], v[98:101]
	v_mfma_f32_16x16x32_bf16 v[70:73], v[168:171], v[224:227], v[70:73]
	v_mfma_f32_16x16x32_bf16 v[66:69], v[176:179], v[224:227], v[66:69]
	s_setprio 0
	s_barrier
	s_add_i32 s30, s53, s40
	v_lshl_add_u64 v[228:229], s[26:27], 0, v[148:149]
	s_mov_b32 m0, s30
	ds_read_b128 v[180:183], v203 offset:16384
	ds_read_b128 v[184:187], v203 offset:17408
	ds_read_b128 v[204:207], v203 offset:18432
	ds_read_b128 v[208:211], v203 offset:19456
	ds_read_b128 v[212:215], v203 offset:20480
	ds_read_b128 v[216:219], v203 offset:21504
	ds_read_b128 v[220:223], v203 offset:22528
	ds_read_b128 v[224:227], v203 offset:23552
	global_load_lds_dwordx4 v[228:229], off
	s_add_i32 m0, s30, 0x2000
	s_add_u32 s30, s26, 0x80000
	v_lshl_add_u64 v[230:231], s[26:27], 0, v[152:153]
	s_addc_u32 s31, s27, 0
	s_add_i32 s34, s54, s40
	global_load_lds_dwordx4 v[230:231], off
	v_lshl_add_u64 v[232:233], s[30:31], 0, v[148:149]
	s_mov_b32 m0, s34
	v_lshl_add_u64 v[234:235], s[28:29], 0, v[150:151]
	global_load_lds_dwordx4 v[232:233], off
	v_lshl_add_u64 v[232:233], s[30:31], 0, v[152:153]
	s_add_i32 m0, s34, 0x2000
	s_nop 0
	global_load_lds_dwordx4 v[232:233], off
	s_waitcnt vmcnt(6)
	s_waitcnt lgkmcnt(0)
	s_barrier
	s_setprio 1
	s_waitcnt lgkmcnt(0)
	v_mfma_f32_16x16x32_bf16 v[62:65], v[74:77], v[180:183], v[62:65]
	v_mfma_f32_16x16x32_bf16 v[58:61], v[82:85], v[180:183], v[58:61]
	v_mfma_f32_16x16x32_bf16 v[46:49], v[74:77], v[204:207], v[46:49]
	v_mfma_f32_16x16x32_bf16 v[42:45], v[82:85], v[204:207], v[42:45]
	v_mfma_f32_16x16x32_bf16 v[30:33], v[74:77], v[212:215], v[30:33]
	v_mfma_f32_16x16x32_bf16 v[26:29], v[82:85], v[212:215], v[26:29]
	v_mfma_f32_16x16x32_bf16 v[14:17], v[74:77], v[220:223], v[14:17]
	v_mfma_f32_16x16x32_bf16 v[10:13], v[82:85], v[220:223], v[10:13]
	v_mfma_f32_16x16x32_bf16 v[62:65], v[78:81], v[184:187], v[62:65]
	v_lshl_add_u64 v[232:233], s[28:29], 0, v[146:147]
	s_mov_b32 m0, s41
	s_nop 0
	global_load_lds_dwordx4 v[232:233], off
	v_mfma_f32_16x16x32_bf16 v[58:61], v[86:89], v[184:187], v[58:61]
	v_mfma_f32_16x16x32_bf16 v[46:49], v[78:81], v[208:211], v[46:49]
	v_mfma_f32_16x16x32_bf16 v[42:45], v[86:89], v[208:211], v[42:45]
	v_mfma_f32_16x16x32_bf16 v[30:33], v[78:81], v[216:219], v[30:33]
	v_mfma_f32_16x16x32_bf16 v[26:29], v[86:89], v[216:219], v[26:29]
	v_mfma_f32_16x16x32_bf16 v[14:17], v[78:81], v[224:227], v[14:17]
	v_mfma_f32_16x16x32_bf16 v[10:13], v[86:89], v[224:227], v[10:13]
	s_setprio 0
	s_setprio 1
	v_mfma_f32_16x16x32_bf16 v[54:57], v[164:167], v[180:183], v[54:57]
	v_mfma_f32_16x16x32_bf16 v[50:53], v[172:175], v[180:183], v[50:53]
	v_mfma_f32_16x16x32_bf16 v[38:41], v[164:167], v[204:207], v[38:41]
	v_mfma_f32_16x16x32_bf16 v[34:37], v[172:175], v[204:207], v[34:37]
	v_mfma_f32_16x16x32_bf16 v[22:25], v[164:167], v[212:215], v[22:25]
	s_mov_b32 m0, s42
	s_nop 0
	global_load_lds_dwordx4 v[234:235], off
	v_mfma_f32_16x16x32_bf16 v[18:21], v[172:175], v[212:215], v[18:21]
	v_mfma_f32_16x16x32_bf16 v[6:9], v[164:167], v[220:223], v[6:9]
	v_mfma_f32_16x16x32_bf16 v[2:5], v[172:175], v[220:223], v[2:5]
	v_mfma_f32_16x16x32_bf16 v[54:57], v[168:171], v[184:187], v[54:57]
	v_mfma_f32_16x16x32_bf16 v[50:53], v[176:179], v[184:187], v[50:53]
	v_mfma_f32_16x16x32_bf16 v[38:41], v[168:171], v[208:211], v[38:41]
	v_mfma_f32_16x16x32_bf16 v[34:37], v[176:179], v[208:211], v[34:37]
	v_mfma_f32_16x16x32_bf16 v[22:25], v[168:171], v[216:219], v[22:25]
	v_mfma_f32_16x16x32_bf16 v[18:21], v[176:179], v[216:219], v[18:21]
	v_mfma_f32_16x16x32_bf16 v[6:9], v[168:171], v[224:227], v[6:9]
	v_mfma_f32_16x16x32_bf16 v[2:5], v[176:179], v[224:227], v[2:5]
	s_setprio 0
	s_barrier
	s_add_i32 s30, 0, 0x18000
	s_add_i32 s31, 0, 0x1c000
	v_add_u32_e32 v86, s30, v200
	v_add_u32_e32 v154, s31, v200
	ds_read_b128 v[74:77], v86
	ds_read_b128 v[78:81], v86 offset:1024
	ds_read_b128 v[82:85], v86 offset:2048
	ds_read_b128 v[86:89], v86 offset:3072
	ds_read_b128 v[164:167], v154
	ds_read_b128 v[168:171], v154 offset:1024
	ds_read_b128 v[172:175], v154 offset:2048
	ds_read_b128 v[176:179], v154 offset:3072
	s_add_u32 s28, s28, 0x80000
	s_addc_u32 s29, s29, 0
	s_mov_b32 m0, s43
	v_lshl_add_u64 v[236:237], s[28:29], 0, v[146:147]
	ds_read_b128 v[180:183], v203 offset:32768
	ds_read_b128 v[184:187], v203 offset:33792
	ds_read_b128 v[204:207], v203 offset:34816
	ds_read_b128 v[208:211], v203 offset:35840
	ds_read_b128 v[212:215], v203 offset:36864
	ds_read_b128 v[216:219], v203 offset:37888
	ds_read_b128 v[220:223], v203 offset:38912
	ds_read_b128 v[224:227], v203 offset:39936
	global_load_lds_dwordx4 v[236:237], off
	v_lshl_add_u64 v[236:237], s[28:29], 0, v[150:151]
	s_mov_b32 m0, s44
	s_nop 0
	global_load_lds_dwordx4 v[236:237], off
	s_waitcnt vmcnt(8)
	s_waitcnt lgkmcnt(0)
	s_barrier
	s_setprio 1
	s_waitcnt lgkmcnt(0)
	v_mfma_f32_16x16x32_bf16 v[142:145], v[74:77], v[180:183], v[142:145]
	v_mfma_f32_16x16x32_bf16 v[138:141], v[82:85], v[180:183], v[138:141]
	v_mfma_f32_16x16x32_bf16 v[126:129], v[74:77], v[204:207], v[126:129]
	v_mfma_f32_16x16x32_bf16 v[122:125], v[82:85], v[204:207], v[122:125]
	v_mfma_f32_16x16x32_bf16 v[110:113], v[74:77], v[212:215], v[110:113]
	v_mfma_f32_16x16x32_bf16 v[106:109], v[82:85], v[212:215], v[106:109]
	v_mfma_f32_16x16x32_bf16 v[94:97], v[74:77], v[220:223], v[94:97]
	v_mfma_f32_16x16x32_bf16 v[90:93], v[82:85], v[220:223], v[90:93]
	v_mfma_f32_16x16x32_bf16 v[142:145], v[78:81], v[184:187], v[142:145]
	v_mfma_f32_16x16x32_bf16 v[138:141], v[86:89], v[184:187], v[138:141]
	v_mfma_f32_16x16x32_bf16 v[126:129], v[78:81], v[208:211], v[126:129]
	v_mfma_f32_16x16x32_bf16 v[122:125], v[86:89], v[208:211], v[122:125]
	v_mfma_f32_16x16x32_bf16 v[110:113], v[78:81], v[216:219], v[110:113]
	v_mfma_f32_16x16x32_bf16 v[106:109], v[86:89], v[216:219], v[106:109]
	v_mfma_f32_16x16x32_bf16 v[94:97], v[78:81], v[224:227], v[94:97]
	v_mfma_f32_16x16x32_bf16 v[90:93], v[86:89], v[224:227], v[90:93]
	s_setprio 0
	s_setprio 1
	v_mfma_f32_16x16x32_bf16 v[134:137], v[164:167], v[180:183], v[134:137]
	v_mfma_f32_16x16x32_bf16 v[130:133], v[172:175], v[180:183], v[130:133]
	v_mfma_f32_16x16x32_bf16 v[118:121], v[164:167], v[204:207], v[118:121]
	v_mfma_f32_16x16x32_bf16 v[114:117], v[172:175], v[204:207], v[114:117]
	v_mfma_f32_16x16x32_bf16 v[102:105], v[164:167], v[212:215], v[102:105]
	v_mfma_f32_16x16x32_bf16 v[98:101], v[172:175], v[212:215], v[98:101]
	v_mfma_f32_16x16x32_bf16 v[70:73], v[164:167], v[220:223], v[70:73]
	v_mfma_f32_16x16x32_bf16 v[66:69], v[172:175], v[220:223], v[66:69]
	v_mfma_f32_16x16x32_bf16 v[134:137], v[168:171], v[184:187], v[134:137]
	v_mfma_f32_16x16x32_bf16 v[130:133], v[176:179], v[184:187], v[130:133]
	v_mfma_f32_16x16x32_bf16 v[118:121], v[168:171], v[208:211], v[118:121]
	v_mfma_f32_16x16x32_bf16 v[114:117], v[176:179], v[208:211], v[114:117]
	v_mfma_f32_16x16x32_bf16 v[102:105], v[168:171], v[216:219], v[102:105]
	v_mfma_f32_16x16x32_bf16 v[98:101], v[176:179], v[216:219], v[98:101]
	v_mfma_f32_16x16x32_bf16 v[70:73], v[168:171], v[224:227], v[70:73]
	v_mfma_f32_16x16x32_bf16 v[66:69], v[176:179], v[224:227], v[66:69]
	s_setprio 0
	s_barrier
	s_add_i32 s28, s30, s40
	v_lshl_add_u64 v[228:229], v[228:229], 0, s[12:13]
	s_mov_b32 m0, s28
	ds_read_b128 v[180:183], v203 offset:49152
	ds_read_b128 v[184:187], v203 offset:50176
	ds_read_b128 v[204:207], v203 offset:51200
	ds_read_b128 v[208:211], v203 offset:52224
	ds_read_b128 v[212:215], v203 offset:53248
	ds_read_b128 v[216:219], v203 offset:54272
	ds_read_b128 v[220:223], v203 offset:55296
	ds_read_b128 v[224:227], v203 offset:56320
	global_load_lds_dwordx4 v[228:229], off
	s_add_i32 m0, s28, 0x2000
	s_add_u32 s26, s26, 0x80080
	v_lshl_add_u64 v[228:229], v[230:231], 0, s[12:13]
	s_addc_u32 s27, s27, 0
	s_add_i32 s28, s31, s40
	global_load_lds_dwordx4 v[228:229], off
	v_lshl_add_u64 v[228:229], s[26:27], 0, v[148:149]
	s_mov_b32 m0, s28
	s_nop 0
	global_load_lds_dwordx4 v[228:229], off
	v_lshl_add_u64 v[228:229], s[26:27], 0, v[152:153]
	s_add_i32 m0, s28, 0x2000
	s_nop 0
	global_load_lds_dwordx4 v[228:229], off
	s_waitcnt vmcnt(6)
	s_waitcnt lgkmcnt(0)
	s_barrier
	s_setprio 1
	s_waitcnt lgkmcnt(0)
	v_mfma_f32_16x16x32_bf16 v[62:65], v[74:77], v[180:183], v[62:65]
	v_mfma_f32_16x16x32_bf16 v[58:61], v[82:85], v[180:183], v[58:61]
	v_mfma_f32_16x16x32_bf16 v[46:49], v[74:77], v[204:207], v[46:49]
	v_mfma_f32_16x16x32_bf16 v[42:45], v[82:85], v[204:207], v[42:45]
	v_mfma_f32_16x16x32_bf16 v[30:33], v[74:77], v[212:215], v[30:33]
	v_mfma_f32_16x16x32_bf16 v[26:29], v[82:85], v[212:215], v[26:29]
	v_mfma_f32_16x16x32_bf16 v[14:17], v[74:77], v[220:223], v[14:17]
	v_mfma_f32_16x16x32_bf16 v[10:13], v[82:85], v[220:223], v[10:13]
	v_mfma_f32_16x16x32_bf16 v[62:65], v[78:81], v[184:187], v[62:65]
	v_lshl_add_u64 v[228:229], v[232:233], 0, s[12:13]
	s_mov_b32 m0, s46
	s_nop 0
	global_load_lds_dwordx4 v[228:229], off
	v_mfma_f32_16x16x32_bf16 v[58:61], v[86:89], v[184:187], v[58:61]
	v_mfma_f32_16x16x32_bf16 v[46:49], v[78:81], v[208:211], v[46:49]
	v_mfma_f32_16x16x32_bf16 v[42:45], v[86:89], v[208:211], v[42:45]
	v_mfma_f32_16x16x32_bf16 v[30:33], v[78:81], v[216:219], v[30:33]
	v_mfma_f32_16x16x32_bf16 v[26:29], v[86:89], v[216:219], v[26:29]
	v_mfma_f32_16x16x32_bf16 v[14:17], v[78:81], v[224:227], v[14:17]
	v_mfma_f32_16x16x32_bf16 v[10:13], v[86:89], v[224:227], v[10:13]
	s_setprio 0
	s_setprio 1
	v_mfma_f32_16x16x32_bf16 v[54:57], v[164:167], v[180:183], v[54:57]
	v_mfma_f32_16x16x32_bf16 v[50:53], v[172:175], v[180:183], v[50:53]
	v_mfma_f32_16x16x32_bf16 v[38:41], v[164:167], v[204:207], v[38:41]
	v_mfma_f32_16x16x32_bf16 v[34:37], v[172:175], v[204:207], v[34:37]
	v_mfma_f32_16x16x32_bf16 v[22:25], v[164:167], v[212:215], v[22:25]
	v_lshl_add_u64 v[228:229], v[234:235], 0, s[12:13]
	s_mov_b32 m0, s47
	s_nop 0
	global_load_lds_dwordx4 v[228:229], off
	v_mfma_f32_16x16x32_bf16 v[18:21], v[172:175], v[212:215], v[18:21]
	v_mfma_f32_16x16x32_bf16 v[6:9], v[164:167], v[220:223], v[6:9]
	v_mfma_f32_16x16x32_bf16 v[2:5], v[172:175], v[220:223], v[2:5]
	v_mfma_f32_16x16x32_bf16 v[54:57], v[168:171], v[184:187], v[54:57]
	v_mfma_f32_16x16x32_bf16 v[50:53], v[176:179], v[184:187], v[50:53]
	v_mfma_f32_16x16x32_bf16 v[38:41], v[168:171], v[208:211], v[38:41]
	v_mfma_f32_16x16x32_bf16 v[34:37], v[176:179], v[208:211], v[34:37]
	v_mfma_f32_16x16x32_bf16 v[22:25], v[168:171], v[216:219], v[22:25]
	v_mfma_f32_16x16x32_bf16 v[18:21], v[176:179], v[216:219], v[18:21]
	v_mfma_f32_16x16x32_bf16 v[6:9], v[168:171], v[224:227], v[6:9]
	v_mfma_f32_16x16x32_bf16 v[2:5], v[176:179], v[224:227], v[2:5]
	s_setprio 0
	s_barrier
	s_add_i32 s19, s19, 2
	s_add_u32 s24, s24, 0x100
	s_addc_u32 s25, s25, 0
	s_add_u32 s7, s7, 0x100
	s_addc_u32 s17, s17, 0
	s_cmp_gt_u32 s19, 29
	s_cbranch_scc0 .LBB0_243
	s_and_b64 vcc, exec, s[14:15]
	s_cbranch_vccz .LBB0_246
	s_barrier

.LBB0_407:
	ds_read_b128 v[150:153], v147
	ds_read_b128 v[154:157], v147 offset:1024
	ds_read_b128 v[158:161], v147 offset:2048
	ds_read_b128 v[162:165], v147 offset:3072
	ds_read_b128 v[166:169], v148
	ds_read_b128 v[170:173], v148 offset:1024
	ds_read_b128 v[174:177], v148 offset:2048
	ds_read_b128 v[178:181], v148 offset:3072
	s_add_u32 s40, s38, 0xfff80080
	s_addc_u32 s41, s39, -1
	s_cmp_eq_u32 s68, 28
	s_cselect_b32 s43, s29, s41
	s_cselect_b32 s42, s28, s40
	s_cselect_b32 s41, s31, s37
	s_cselect_b32 s40, s30, s27
	v_lshl_add_u64 v[214:215], s[38:39], 0, v[140:141]
	s_add_i32 m0, s47, 0xc000
	ds_read_b128 v[182:185], v149
	ds_read_b128 v[186:189], v149 offset:1024
	ds_read_b128 v[190:193], v149 offset:2048
	ds_read_b128 v[194:197], v149 offset:3072
	ds_read_b128 v[198:201], v149 offset:4096
	ds_read_b128 v[202:205], v149 offset:5120
	ds_read_b128 v[206:209], v149 offset:6144
	ds_read_b128 v[210:213], v149 offset:7168
	global_load_lds_dwordx4 v[214:215], off
	v_lshl_add_u64 v[214:215], s[38:39], 0, v[142:143]
	s_add_i32 m0, s47, 0xe000
	s_nop 0
	global_load_lds_dwordx4 v[214:215], off
	s_waitcnt vmcnt(8)
	s_waitcnt lgkmcnt(0)
	s_barrier
	s_setprio 1
	s_waitcnt lgkmcnt(0)
	v_mfma_f32_16x16x32_bf16 v[126:129], v[150:153], v[182:185], v[126:129]
	v_mfma_f32_16x16x32_bf16 v[122:125], v[158:161], v[182:185], v[122:125]
	v_mfma_f32_16x16x32_bf16 v[118:121], v[150:153], v[190:193], v[118:121]
	v_mfma_f32_16x16x32_bf16 v[114:117], v[158:161], v[190:193], v[114:117]
	v_mfma_f32_16x16x32_bf16 v[110:113], v[150:153], v[198:201], v[110:113]
	v_mfma_f32_16x16x32_bf16 v[102:105], v[158:161], v[198:201], v[102:105]
	v_mfma_f32_16x16x32_bf16 v[86:89], v[150:153], v[206:209], v[86:89]
	v_mfma_f32_16x16x32_bf16 v[74:77], v[158:161], v[206:209], v[74:77]
	v_mfma_f32_16x16x32_bf16 v[126:129], v[154:157], v[186:189], v[126:129]
	v_mfma_f32_16x16x32_bf16 v[122:125], v[162:165], v[186:189], v[122:125]
	v_mfma_f32_16x16x32_bf16 v[118:121], v[154:157], v[194:197], v[118:121]
	v_mfma_f32_16x16x32_bf16 v[114:117], v[162:165], v[194:197], v[114:117]
	v_mfma_f32_16x16x32_bf16 v[110:113], v[154:157], v[202:205], v[110:113]
	v_mfma_f32_16x16x32_bf16 v[102:105], v[162:165], v[202:205], v[102:105]
	v_mfma_f32_16x16x32_bf16 v[86:89], v[154:157], v[210:213], v[86:89]
	v_mfma_f32_16x16x32_bf16 v[74:77], v[162:165], v[210:213], v[74:77]
	s_setprio 0
	s_setprio 1
	v_mfma_f32_16x16x32_bf16 v[106:109], v[166:169], v[182:185], v[106:109]
	v_mfma_f32_16x16x32_bf16 v[98:101], v[174:177], v[182:185], v[98:101]
	v_mfma_f32_16x16x32_bf16 v[94:97], v[166:169], v[190:193], v[94:97]
	v_mfma_f32_16x16x32_bf16 v[90:93], v[174:177], v[190:193], v[90:93]
	v_mfma_f32_16x16x32_bf16 v[82:85], v[166:169], v[198:201], v[82:85]
	v_mfma_f32_16x16x32_bf16 v[78:81], v[174:177], v[198:201], v[78:81]
	v_mfma_f32_16x16x32_bf16 v[70:73], v[166:169], v[206:209], v[70:73]
	v_mfma_f32_16x16x32_bf16 v[66:69], v[174:177], v[206:209], v[66:69]
	v_mfma_f32_16x16x32_bf16 v[106:109], v[170:173], v[186:189], v[106:109]
	v_mfma_f32_16x16x32_bf16 v[98:101], v[178:181], v[186:189], v[98:101]
	v_mfma_f32_16x16x32_bf16 v[94:97], v[170:173], v[194:197], v[94:97]
	v_mfma_f32_16x16x32_bf16 v[90:93], v[178:181], v[194:197], v[90:93]
	v_mfma_f32_16x16x32_bf16 v[82:85], v[170:173], v[202:205], v[82:85]
	v_mfma_f32_16x16x32_bf16 v[78:81], v[178:181], v[202:205], v[78:81]
	v_mfma_f32_16x16x32_bf16 v[70:73], v[170:173], v[210:213], v[70:73]
	v_mfma_f32_16x16x32_bf16 v[66:69], v[178:181], v[210:213], v[66:69]
	s_setprio 0
	s_barrier
	s_add_i32 s69, s57, s3
	v_lshl_add_u64 v[214:215], s[40:41], 0, v[134:135]
	s_mov_b32 m0, s69
	ds_read_b128 v[182:185], v149 offset:16384
	ds_read_b128 v[186:189], v149 offset:17408
	ds_read_b128 v[190:193], v149 offset:18432
	ds_read_b128 v[194:197], v149 offset:19456
	ds_read_b128 v[198:201], v149 offset:20480
	ds_read_b128 v[202:205], v149 offset:21504
	ds_read_b128 v[206:209], v149 offset:22528
	ds_read_b128 v[210:213], v149 offset:23552
	global_load_lds_dwordx4 v[214:215], off
	s_add_i32 m0, s69, 0x2000
	s_add_u32 s70, s40, 0x80000
	v_lshl_add_u64 v[216:217], s[40:41], 0, v[130:131]
	s_addc_u32 s71, s41, 0
	s_add_i32 s69, s58, s3
	global_load_lds_dwordx4 v[216:217], off
	v_lshl_add_u64 v[218:219], s[70:71], 0, v[134:135]
	s_mov_b32 m0, s69
	v_lshl_add_u64 v[220:221], s[42:43], 0, v[132:133]
	global_load_lds_dwordx4 v[218:219], off
	v_lshl_add_u64 v[218:219], s[70:71], 0, v[130:131]
	s_add_i32 m0, s69, 0x2000
	s_nop 0
	global_load_lds_dwordx4 v[218:219], off
	s_waitcnt vmcnt(6)
	s_waitcnt lgkmcnt(0)
	s_barrier
	s_setprio 1
	s_waitcnt lgkmcnt(0)
	v_mfma_f32_16x16x32_bf16 v[62:65], v[150:153], v[182:185], v[62:65]
	v_mfma_f32_16x16x32_bf16 v[58:61], v[158:161], v[182:185], v[58:61]
	v_mfma_f32_16x16x32_bf16 v[54:57], v[150:153], v[190:193], v[54:57]
	v_mfma_f32_16x16x32_bf16 v[46:49], v[158:161], v[190:193], v[46:49]
	v_mfma_f32_16x16x32_bf16 v[38:41], v[150:153], v[198:201], v[38:41]
	v_mfma_f32_16x16x32_bf16 v[30:33], v[158:161], v[198:201], v[30:33]
	v_mfma_f32_16x16x32_bf16 v[22:25], v[150:153], v[206:209], v[22:25]
	v_mfma_f32_16x16x32_bf16 v[14:17], v[158:161], v[206:209], v[14:17]
	v_mfma_f32_16x16x32_bf16 v[62:65], v[154:157], v[186:189], v[62:65]
	v_lshl_add_u64 v[218:219], s[42:43], 0, v[136:137]
	s_mov_b32 m0, s47
	s_nop 0
	global_load_lds_dwordx4 v[218:219], off
	v_mfma_f32_16x16x32_bf16 v[58:61], v[162:165], v[186:189], v[58:61]
	v_mfma_f32_16x16x32_bf16 v[54:57], v[154:157], v[194:197], v[54:57]
	v_mfma_f32_16x16x32_bf16 v[46:49], v[162:165], v[194:197], v[46:49]
	v_mfma_f32_16x16x32_bf16 v[38:41], v[154:157], v[202:205], v[38:41]
	v_mfma_f32_16x16x32_bf16 v[30:33], v[162:165], v[202:205], v[30:33]
	v_mfma_f32_16x16x32_bf16 v[22:25], v[154:157], v[210:213], v[22:25]
	v_mfma_f32_16x16x32_bf16 v[14:17], v[162:165], v[210:213], v[14:17]
	s_setprio 0
	s_setprio 1
	v_mfma_f32_16x16x32_bf16 v[50:53], v[166:169], v[182:185], v[50:53]
	v_mfma_f32_16x16x32_bf16 v[42:45], v[174:177], v[182:185], v[42:45]
	v_mfma_f32_16x16x32_bf16 v[34:37], v[166:169], v[190:193], v[34:37]
	v_mfma_f32_16x16x32_bf16 v[26:29], v[174:177], v[190:193], v[26:29]
	v_mfma_f32_16x16x32_bf16 v[18:21], v[166:169], v[198:201], v[18:21]
	s_mov_b32 m0, s48
	s_nop 0
	global_load_lds_dwordx4 v[220:221], off
	v_mfma_f32_16x16x32_bf16 v[10:13], v[174:177], v[198:201], v[10:13]
	v_mfma_f32_16x16x32_bf16 v[6:9], v[166:169], v[206:209], v[6:9]
	v_mfma_f32_16x16x32_bf16 v[2:5], v[174:177], v[206:209], v[2:5]
	v_mfma_f32_16x16x32_bf16 v[50:53], v[170:173], v[186:189], v[50:53]
	v_mfma_f32_16x16x32_bf16 v[42:45], v[178:181], v[186:189], v[42:45]
	v_mfma_f32_16x16x32_bf16 v[34:37], v[170:173], v[194:197], v[34:37]
	v_mfma_f32_16x16x32_bf16 v[26:29], v[178:181], v[194:197], v[26:29]
	v_mfma_f32_16x16x32_bf16 v[18:21], v[170:173], v[202:205], v[18:21]
	v_mfma_f32_16x16x32_bf16 v[10:13], v[178:181], v[202:205], v[10:13]
	v_mfma_f32_16x16x32_bf16 v[6:9], v[170:173], v[210:213], v[6:9]
	v_mfma_f32_16x16x32_bf16 v[2:5], v[178:181], v[210:213], v[2:5]
	s_setprio 0
	s_barrier
	s_add_i32 s69, 0, 0x18000
	v_add_u32_e32 v138, s69, v145
	s_add_i32 s70, 0, 0x1c000
	ds_read_b128 v[150:153], v138
	ds_read_b128 v[154:157], v138 offset:1024
	ds_read_b128 v[158:161], v138 offset:2048
	ds_read_b128 v[162:165], v138 offset:3072
	v_add_u32_e32 v138, s70, v145
	ds_read_b128 v[166:169], v138
	ds_read_b128 v[170:173], v138 offset:1024
	ds_read_b128 v[174:177], v138 offset:2048
	ds_read_b128 v[178:181], v138 offset:3072
	s_add_u32 s42, s42, 0x80000
	s_addc_u32 s43, s43, 0
	s_mov_b32 m0, s49
	v_lshl_add_u64 v[222:223], s[42:43], 0, v[136:137]
	ds_read_b128 v[182:185], v149 offset:32768
	ds_read_b128 v[186:189], v149 offset:33792
	ds_read_b128 v[190:193], v149 offset:34816
	ds_read_b128 v[194:197], v149 offset:35840
	ds_read_b128 v[198:201], v149 offset:36864
	ds_read_b128 v[202:205], v149 offset:37888
	ds_read_b128 v[206:209], v149 offset:38912
	ds_read_b128 v[210:213], v149 offset:39936
	global_load_lds_dwordx4 v[222:223], off
	v_lshl_add_u64 v[222:223], s[42:43], 0, v[132:133]
	s_mov_b32 m0, s50
	s_nop 0
	global_load_lds_dwordx4 v[222:223], off
	s_waitcnt vmcnt(8)
	s_waitcnt lgkmcnt(0)
	s_barrier
	s_setprio 1
	s_waitcnt lgkmcnt(0)
	v_mfma_f32_16x16x32_bf16 v[126:129], v[150:153], v[182:185], v[126:129]
	v_mfma_f32_16x16x32_bf16 v[122:125], v[158:161], v[182:185], v[122:125]
	v_mfma_f32_16x16x32_bf16 v[118:121], v[150:153], v[190:193], v[118:121]
	v_mfma_f32_16x16x32_bf16 v[114:117], v[158:161], v[190:193], v[114:117]
	v_mfma_f32_16x16x32_bf16 v[110:113], v[150:153], v[198:201], v[110:113]
	v_mfma_f32_16x16x32_bf16 v[102:105], v[158:161], v[198:201], v[102:105]
	v_mfma_f32_16x16x32_bf16 v[86:89], v[150:153], v[206:209], v[86:89]
	v_mfma_f32_16x16x32_bf16 v[74:77], v[158:161], v[206:209], v[74:77]
	v_mfma_f32_16x16x32_bf16 v[126:129], v[154:157], v[186:189], v[126:129]
	v_mfma_f32_16x16x32_bf16 v[122:125], v[162:165], v[186:189], v[122:125]
	v_mfma_f32_16x16x32_bf16 v[118:121], v[154:157], v[194:197], v[118:121]
	v_mfma_f32_16x16x32_bf16 v[114:117], v[162:165], v[194:197], v[114:117]
	v_mfma_f32_16x16x32_bf16 v[110:113], v[154:157], v[202:205], v[110:113]
	v_mfma_f32_16x16x32_bf16 v[102:105], v[162:165], v[202:205], v[102:105]
	v_mfma_f32_16x16x32_bf16 v[86:89], v[154:157], v[210:213], v[86:89]
	v_mfma_f32_16x16x32_bf16 v[74:77], v[162:165], v[210:213], v[74:77]
	s_setprio 0
	s_setprio 1
	v_mfma_f32_16x16x32_bf16 v[106:109], v[166:169], v[182:185], v[106:109]
	v_mfma_f32_16x16x32_bf16 v[98:101], v[174:177], v[182:185], v[98:101]
	v_mfma_f32_16x16x32_bf16 v[94:97], v[166:169], v[190:193], v[94:97]
	v_mfma_f32_16x16x32_bf16 v[90:93], v[174:177], v[190:193], v[90:93]
	v_mfma_f32_16x16x32_bf16 v[82:85], v[166:169], v[198:201], v[82:85]
	v_mfma_f32_16x16x32_bf16 v[78:81], v[174:177], v[198:201], v[78:81]
	v_mfma_f32_16x16x32_bf16 v[70:73], v[166:169], v[206:209], v[70:73]
	v_mfma_f32_16x16x32_bf16 v[66:69], v[174:177], v[206:209], v[66:69]
	v_mfma_f32_16x16x32_bf16 v[106:109], v[170:173], v[186:189], v[106:109]
	v_mfma_f32_16x16x32_bf16 v[98:101], v[178:181], v[186:189], v[98:101]
	v_mfma_f32_16x16x32_bf16 v[94:97], v[170:173], v[194:197], v[94:97]
	v_mfma_f32_16x16x32_bf16 v[90:93], v[178:181], v[194:197], v[90:93]
	v_mfma_f32_16x16x32_bf16 v[82:85], v[170:173], v[202:205], v[82:85]
	v_mfma_f32_16x16x32_bf16 v[78:81], v[178:181], v[202:205], v[78:81]
	v_mfma_f32_16x16x32_bf16 v[70:73], v[170:173], v[210:213], v[70:73]
	v_mfma_f32_16x16x32_bf16 v[66:69], v[178:181], v[210:213], v[66:69]
	s_setprio 0
	s_barrier
	s_add_i32 s42, s69, s3
	v_lshl_add_u64 v[214:215], v[214:215], 0, s[16:17]
	s_mov_b32 m0, s42
	ds_read_b128 v[182:185], v149 offset:49152
	ds_read_b128 v[186:189], v149 offset:50176
	ds_read_b128 v[190:193], v149 offset:51200
	ds_read_b128 v[194:197], v149 offset:52224
	ds_read_b128 v[198:201], v149 offset:53248
	ds_read_b128 v[202:205], v149 offset:54272
	ds_read_b128 v[206:209], v149 offset:55296
	ds_read_b128 v[210:213], v149 offset:56320
	global_load_lds_dwordx4 v[214:215], off
	s_add_i32 m0, s42, 0x2000
	s_add_u32 s40, s40, 0x80080
	v_lshl_add_u64 v[214:215], v[216:217], 0, s[16:17]
	s_addc_u32 s41, s41, 0
	s_add_i32 s42, s70, s3
	global_load_lds_dwordx4 v[214:215], off
	v_lshl_add_u64 v[214:215], s[40:41], 0, v[134:135]
	s_mov_b32 m0, s42
	s_nop 0
	global_load_lds_dwordx4 v[214:215], off
	v_lshl_add_u64 v[214:215], s[40:41], 0, v[130:131]
	s_add_i32 m0, s42, 0x2000
	s_nop 0
	global_load_lds_dwordx4 v[214:215], off
	s_waitcnt vmcnt(6)
	s_waitcnt lgkmcnt(0)
	s_barrier
	s_setprio 1
	s_waitcnt lgkmcnt(0)
	v_mfma_f32_16x16x32_bf16 v[62:65], v[150:153], v[182:185], v[62:65]
	v_mfma_f32_16x16x32_bf16 v[58:61], v[158:161], v[182:185], v[58:61]
	v_mfma_f32_16x16x32_bf16 v[54:57], v[150:153], v[190:193], v[54:57]
	v_mfma_f32_16x16x32_bf16 v[46:49], v[158:161], v[190:193], v[46:49]
	v_mfma_f32_16x16x32_bf16 v[38:41], v[150:153], v[198:201], v[38:41]
	v_mfma_f32_16x16x32_bf16 v[30:33], v[158:161], v[198:201], v[30:33]
	v_mfma_f32_16x16x32_bf16 v[22:25], v[150:153], v[206:209], v[22:25]
	v_mfma_f32_16x16x32_bf16 v[14:17], v[158:161], v[206:209], v[14:17]
	v_mfma_f32_16x16x32_bf16 v[62:65], v[154:157], v[186:189], v[62:65]
	v_lshl_add_u64 v[214:215], v[218:219], 0, s[16:17]
	s_mov_b32 m0, s55
	s_nop 0
	global_load_lds_dwordx4 v[214:215], off
	v_mfma_f32_16x16x32_bf16 v[58:61], v[162:165], v[186:189], v[58:61]
	v_mfma_f32_16x16x32_bf16 v[54:57], v[154:157], v[194:197], v[54:57]
	v_mfma_f32_16x16x32_bf16 v[46:49], v[162:165], v[194:197], v[46:49]
	v_mfma_f32_16x16x32_bf16 v[38:41], v[154:157], v[202:205], v[38:41]
	v_mfma_f32_16x16x32_bf16 v[30:33], v[162:165], v[202:205], v[30:33]
	v_mfma_f32_16x16x32_bf16 v[22:25], v[154:157], v[210:213], v[22:25]
	v_mfma_f32_16x16x32_bf16 v[14:17], v[162:165], v[210:213], v[14:17]
	s_setprio 0
	s_setprio 1
	v_mfma_f32_16x16x32_bf16 v[50:53], v[166:169], v[182:185], v[50:53]
	v_mfma_f32_16x16x32_bf16 v[42:45], v[174:177], v[182:185], v[42:45]
	v_mfma_f32_16x16x32_bf16 v[34:37], v[166:169], v[190:193], v[34:37]
	v_mfma_f32_16x16x32_bf16 v[26:29], v[174:177], v[190:193], v[26:29]
	v_mfma_f32_16x16x32_bf16 v[18:21], v[166:169], v[198:201], v[18:21]
	v_lshl_add_u64 v[214:215], v[220:221], 0, s[16:17]
	s_mov_b32 m0, s56
	s_nop 0
	global_load_lds_dwordx4 v[214:215], off
	v_mfma_f32_16x16x32_bf16 v[10:13], v[174:177], v[198:201], v[10:13]
	v_mfma_f32_16x16x32_bf16 v[6:9], v[166:169], v[206:209], v[6:9]
	v_mfma_f32_16x16x32_bf16 v[2:5], v[174:177], v[206:209], v[2:5]
	v_mfma_f32_16x16x32_bf16 v[50:53], v[170:173], v[186:189], v[50:53]
	v_mfma_f32_16x16x32_bf16 v[42:45], v[178:181], v[186:189], v[42:45]
	v_mfma_f32_16x16x32_bf16 v[34:37], v[170:173], v[194:197], v[34:37]
	v_mfma_f32_16x16x32_bf16 v[26:29], v[178:181], v[194:197], v[26:29]
	v_mfma_f32_16x16x32_bf16 v[18:21], v[170:173], v[202:205], v[18:21]
	v_mfma_f32_16x16x32_bf16 v[10:13], v[178:181], v[202:205], v[10:13]
	v_mfma_f32_16x16x32_bf16 v[6:9], v[170:173], v[210:213], v[6:9]
	v_mfma_f32_16x16x32_bf16 v[2:5], v[178:181], v[210:213], v[2:5]
	s_setprio 0
	s_barrier
	s_add_i32 s68, s68, 2
	s_add_u32 s38, s38, 0x100
	s_addc_u32 s39, s39, 0
	s_add_u32 s27, s27, 0x100
	s_addc_u32 s37, s37, 0
	s_cmp_gt_u32 s68, 29
	s_cbranch_scc0 .LBB0_407
	s_and_b64 vcc, exec, s[18:19]
	s_cbranch_vccz .LBB0_410
	s_barrier
